# speedup vs baseline: 1.0011x; 1.0011x over previous
.LBB2_12:
	s_or_b64 exec, exec, s[12:13]
	v_lshlrev_b32_e32 v106, 9, v119
	v_ffbl_b32_e32 v107, v107
	v_ffbl_b32_e32 v108, v108
	v_lshlrev_b32_e32 v116, 25, v119
	v_lshl_or_b32 v107, v107, 4, v106
	v_mov_b32_e32 v109, 0x2000
	v_lshl_or_b32 v108, v108, 20, v116
	v_bfrev_b32_e32 v116, 4
	v_ffbl_b32_e32 v0, v0
	v_cndmask_b32_e64 v107, v107, v109, s[8:9]
	v_cndmask_b32_e64 v108, v108, v116, s[4:5]
	v_lshl_or_b32 v0, v0, 4, v106
	v_cndmask_b32_e32 v0, v0, v109, vcc
	v_or_b32_e32 v106, v108, v107
	v_mov_b32_e32 v108, 0x800000
	v_lshlrev_b32_e32 v107, 16, v117
	v_cndmask_b32_e64 v108, 0, v108, s[6:7]
	s_waitcnt lgkmcnt(2)
	v_lshl_or_b32 v0, v118, 24, v0
	v_or3_b32 v0, v0, v108, v107
	ds_write2_b32 v105, v106, v0 offset0:1 offset1:3
	v_cmp_ne_u32_e32 vcc, 0, v140
	v_cmp_ne_u32_e64 s[22:23], 0, v141
	v_lshlrev_b32_e32 v150, 5, v113
	v_lshl_add_u32 v155, v113, 2, v115
	v_lshlrev_b32_e32 v155, 2, v155
	v_add_u32_e32 v155, 0x11840, v155
	v_lshrrev_b64 v[146:147], v150, vcc
	v_lshrrev_b64 v[156:157], v150, s[22:23]
	v_mov_b32_e32 v151, 0x400
	v_cmp_ne_u32_e32 vcc, 0, v146
	v_cmp_ne_u32_e64 s[22:23], 0, v156
	s_nop 1
	v_cndmask_b32_e32 v146, 0, v151, vcc
	v_cndmask_b32_e64 v156, 0, v151, s[22:23]
	v_cmp_eq_u32_e32 vcc, 0, v111
	s_and_saveexec_b64 s[22:23], vcc
	ds_or_b32 v155, v146
	ds_or_b32 v155, v156 offset:32
	s_or_b64 exec, exec, s[22:23]
	s_movk_i32 s2, 0x2010
	v_mul_u32_u24_e32 v105, 0x2010, v115
	v_cmp_eq_u32_e32 vcc, 0, v114
	s_waitcnt vmcnt(22)
	ds_write_b128 v104, v[38:41] offset:32832
	s_waitcnt vmcnt(21)
	ds_write_b128 v104, v[42:45] offset:36928
	s_waitcnt vmcnt(20)
	ds_write_b128 v104, v[46:49] offset:41024
	s_waitcnt vmcnt(19)
	ds_write_b128 v104, v[50:53] offset:45120
	s_waitcnt vmcnt(18)
	ds_write_b128 v104, v[54:57] offset:49216
	s_waitcnt vmcnt(17)
	ds_write_b128 v104, v[66:69] offset:53312
	s_and_saveexec_b64 s[0:1], vcc
	v_mov_b32_e32 v38, 0
	v_mov_b32_e32 v39, v38
	v_mov_b32_e32 v40, v38
	v_mov_b32_e32 v41, v38
	ds_write_b128 v105, v[38:41] offset:8192
	s_or_b64 exec, exec, s[0:1]
	v_lshlrev_b32_e32 v40, 3, v113
	v_lshlrev_b32_e32 v67, 4, v110
	v_or_b32_e32 v38, 0x1e0, v111
	v_or_b32_e32 v0, 0x8040, v40
	v_mad_u32_u24 v66, v1, s2, v67
	v_mad_u32_u24 v38, v38, 48, v0
	s_waitcnt vmcnt(16)
	ds_write_b128 v66, v[58:61]
	s_waitcnt vmcnt(15)
	ds_write_b128 v66, v[62:65] offset:1024
	s_waitcnt vmcnt(14)
	ds_write_b128 v66, v[70:73] offset:2048
	s_waitcnt vmcnt(13)
	ds_write_b128 v66, v[74:77] offset:3072
	s_waitcnt vmcnt(12)
	ds_write_b128 v66, v[78:81] offset:4096
	s_waitcnt vmcnt(11)
	ds_write_b128 v66, v[82:85] offset:5120
	s_waitcnt vmcnt(10)
	ds_write_b128 v66, v[86:89] offset:6144
	s_waitcnt vmcnt(9)
	ds_write_b128 v66, v[90:93] offset:7168
	s_waitcnt lgkmcnt(0)
	s_barrier
	v_readfirstlane_b32 s31, v115
	s_cmp_eq_u32 s31, 0
	s_cbranch_scc1 .Lstag_done
	s_sleep 1
	s_cmp_eq_u32 s31, 1
	s_cbranch_scc1 .Lstag_done
	s_sleep 1
	s_cmp_eq_u32 s31, 2
	s_cbranch_scc1 .Lstag_done
	s_sleep 1
